# v75 + prologue pool-weight fold: a thread's 128 mix values loaded once, w_in rows streamed through register buffers (same f32 FMA order)
# speedup vs baseline: 1.0034x; 1.0034x over previous
; __device__ __forceinline__ bf16_t f2bf(float f) { unsigned u = __float_as_uint(f); return (bf16_t)((u + 0x7fffu + ((u >> 16) & 1u)) >> 16); }
; __device__ __forceinline__ void ph_prologue(const Args& a, LAS unsigned char* lds) {
;     ...
;         const float* win = a.in[1]; const float* mix = a.in[2]; const float* psc = a.in[3]; bf16_t* WIN0 = (bf16_t*)(a.ws + WS_WIN0);
;         for (int i = gt; i < 512 * 1024; i += ngt) { const int n = i & 511, k = i >> 9, g = n >> 7, nn = n & 127;
;             const float* wr_ = win + (size_t)k * 1536 + g * 128; const float* mx = mix + (size_t)g * 128 * 128 + nn;
;             float s = 0.f;
;             for (int c = 0; c < 128; ++c) s += wr_[c] * mx[(size_t)c * 128];
;             WIN0[(size_t)n * 1024 + k] = f2bf(s * psc[n]); }
.LBB0_90:
	s_or_b64 exec, exec, s[4:5]
	s_cmp_lg_u32 s22, 0x100
	s_cbranch_scc1 .Lfold_orig
	s_load_dwordx4 s[8:11], s[82:83], 0x10
	s_load_dwordx2 s[6:7], s[82:83], 0x8
	v_lshlrev_b32_e32 v2, 2, v0
	v_lshrrev_b32_e32 v3, 7, v0
	v_and_b32_e32 v4, 0x7f, v0
	v_lshlrev_b32_e32 v5, 16, v3
	v_lshl_or_b32 v5, v4, 2, v5
	v_lshlrev_b32_e32 v9, 9, v3
	v_lshlrev_b32_e32 v10, 11, v0
	s_add_u32 s12, s0, 0x3db00000
	s_addc_u32 s13, s1, 0
	s_movk_i32 s14, 0x7fff
	v_readlane_b32 s15, v252, 6
	s_waitcnt lgkmcnt(0)
	global_load_dword v7, v2, s[10:11]
	global_load_dword v124, v5, s[8:9]
	global_load_dword v125, v5, s[8:9] offset:512
	global_load_dword v126, v5, s[8:9] offset:1024
	global_load_dword v127, v5, s[8:9] offset:1536
	global_load_dword v128, v5, s[8:9] offset:2048
	global_load_dword v129, v5, s[8:9] offset:2560
	global_load_dword v130, v5, s[8:9] offset:3072
	global_load_dword v131, v5, s[8:9] offset:3584
	s_add_u32 s8, s8, 0x1000
	s_addc_u32 s9, s9, 0
	global_load_dword v132, v5, s[8:9]
	global_load_dword v133, v5, s[8:9] offset:512
	global_load_dword v134, v5, s[8:9] offset:1024
	global_load_dword v135, v5, s[8:9] offset:1536
	global_load_dword v136, v5, s[8:9] offset:2048
	global_load_dword v137, v5, s[8:9] offset:2560
	global_load_dword v138, v5, s[8:9] offset:3072
	global_load_dword v139, v5, s[8:9] offset:3584
	s_add_u32 s8, s8, 0x1000
	s_addc_u32 s9, s9, 0
	global_load_dword v140, v5, s[8:9]
	global_load_dword v141, v5, s[8:9] offset:512
	global_load_dword v142, v5, s[8:9] offset:1024
	global_load_dword v143, v5, s[8:9] offset:1536
	global_load_dword v144, v5, s[8:9] offset:2048
	global_load_dword v145, v5, s[8:9] offset:2560
	global_load_dword v146, v5, s[8:9] offset:3072
	global_load_dword v147, v5, s[8:9] offset:3584
	s_add_u32 s8, s8, 0x1000
	s_addc_u32 s9, s9, 0
	global_load_dword v148, v5, s[8:9]
	global_load_dword v149, v5, s[8:9] offset:512
	global_load_dword v150, v5, s[8:9] offset:1024
	global_load_dword v151, v5, s[8:9] offset:1536
	global_load_dword v152, v5, s[8:9] offset:2048
	global_load_dword v153, v5, s[8:9] offset:2560
	global_load_dword v154, v5, s[8:9] offset:3072
	global_load_dword v155, v5, s[8:9] offset:3584
	s_add_u32 s8, s8, 0x1000
	s_addc_u32 s9, s9, 0
	global_load_dword v156, v5, s[8:9]
	global_load_dword v157, v5, s[8:9] offset:512
	global_load_dword v158, v5, s[8:9] offset:1024
	global_load_dword v159, v5, s[8:9] offset:1536
	global_load_dword v160, v5, s[8:9] offset:2048
	global_load_dword v161, v5, s[8:9] offset:2560
	global_load_dword v162, v5, s[8:9] offset:3072
	global_load_dword v163, v5, s[8:9] offset:3584
	s_add_u32 s8, s8, 0x1000
	s_addc_u32 s9, s9, 0
	global_load_dword v164, v5, s[8:9]
	global_load_dword v165, v5, s[8:9] offset:512
	global_load_dword v166, v5, s[8:9] offset:1024
	global_load_dword v167, v5, s[8:9] offset:1536
	global_load_dword v168, v5, s[8:9] offset:2048
	global_load_dword v169, v5, s[8:9] offset:2560
	global_load_dword v170, v5, s[8:9] offset:3072
	global_load_dword v171, v5, s[8:9] offset:3584
	s_add_u32 s8, s8, 0x1000
	s_addc_u32 s9, s9, 0
	global_load_dword v172, v5, s[8:9]
	global_load_dword v173, v5, s[8:9] offset:512
	global_load_dword v174, v5, s[8:9] offset:1024
	global_load_dword v175, v5, s[8:9] offset:1536
	global_load_dword v176, v5, s[8:9] offset:2048
	global_load_dword v177, v5, s[8:9] offset:2560
	global_load_dword v178, v5, s[8:9] offset:3072
	global_load_dword v179, v5, s[8:9] offset:3584
	s_add_u32 s8, s8, 0x1000
	s_addc_u32 s9, s9, 0
	global_load_dword v180, v5, s[8:9]
	global_load_dword v181, v5, s[8:9] offset:512
	global_load_dword v182, v5, s[8:9] offset:1024
	global_load_dword v183, v5, s[8:9] offset:1536
	global_load_dword v184, v5, s[8:9] offset:2048
	global_load_dword v185, v5, s[8:9] offset:2560
	global_load_dword v186, v5, s[8:9] offset:3072
	global_load_dword v187, v5, s[8:9] offset:3584
	s_add_u32 s8, s8, 0x1000
	s_addc_u32 s9, s9, 0
	global_load_dword v188, v5, s[8:9]
	global_load_dword v189, v5, s[8:9] offset:512
	global_load_dword v190, v5, s[8:9] offset:1024
	global_load_dword v191, v5, s[8:9] offset:1536
	global_load_dword v192, v5, s[8:9] offset:2048
	global_load_dword v193, v5, s[8:9] offset:2560
	global_load_dword v194, v5, s[8:9] offset:3072
	global_load_dword v195, v5, s[8:9] offset:3584
	s_add_u32 s8, s8, 0x1000
	s_addc_u32 s9, s9, 0
	global_load_dword v196, v5, s[8:9]
	global_load_dword v197, v5, s[8:9] offset:512
	global_load_dword v198, v5, s[8:9] offset:1024
	global_load_dword v199, v5, s[8:9] offset:1536
	global_load_dword v200, v5, s[8:9] offset:2048
	global_load_dword v201, v5, s[8:9] offset:2560
	global_load_dword v202, v5, s[8:9] offset:3072
	global_load_dword v203, v5, s[8:9] offset:3584
	s_add_u32 s8, s8, 0x1000
	s_addc_u32 s9, s9, 0
	global_load_dword v204, v5, s[8:9]
	global_load_dword v205, v5, s[8:9] offset:512
	global_load_dword v206, v5, s[8:9] offset:1024
	global_load_dword v207, v5, s[8:9] offset:1536
	global_load_dword v208, v5, s[8:9] offset:2048
	global_load_dword v209, v5, s[8:9] offset:2560
	global_load_dword v210, v5, s[8:9] offset:3072
	global_load_dword v211, v5, s[8:9] offset:3584
	s_add_u32 s8, s8, 0x1000
	s_addc_u32 s9, s9, 0
	global_load_dword v212, v5, s[8:9]
	global_load_dword v213, v5, s[8:9] offset:512
	global_load_dword v214, v5, s[8:9] offset:1024
	global_load_dword v215, v5, s[8:9] offset:1536
	global_load_dword v216, v5, s[8:9] offset:2048
	global_load_dword v217, v5, s[8:9] offset:2560
	global_load_dword v218, v5, s[8:9] offset:3072
	global_load_dword v219, v5, s[8:9] offset:3584
	s_add_u32 s8, s8, 0x1000
	s_addc_u32 s9, s9, 0
	global_load_dword v220, v5, s[8:9]
	global_load_dword v221, v5, s[8:9] offset:512
; __device__ __forceinline__ bf16_t f2bf(float f) { unsigned u = __float_as_uint(f); return (bf16_t)((u + 0x7fffu + ((u >> 16) & 1u)) >> 16); }
; __device__ __forceinline__ void ph_prologue(const Args& a, LAS unsigned char* lds) {
;     ...
;         const float* win = a.in[1]; const float* mix = a.in[2]; const float* psc = a.in[3]; bf16_t* WIN0 = (bf16_t*)(a.ws + WS_WIN0);
;         for (int i = gt; i < 512 * 1024; i += ngt) { const int n = i & 511, k = i >> 9, g = n >> 7, nn = n & 127;
;             const float* wr_ = win + (size_t)k * 1536 + g * 128; const float* mx = mix + (size_t)g * 128 * 128 + nn;
;             float s = 0.f;
;             for (int c = 0; c < 128; ++c) s += wr_[c] * mx[(size_t)c * 128];
;             WIN0[(size_t)n * 1024 + k] = f2bf(s * psc[n]); }
	global_load_dword v222, v5, s[8:9] offset:1024
	global_load_dword v223, v5, s[8:9] offset:1536
	global_load_dword v224, v5, s[8:9] offset:2048
	global_load_dword v225, v5, s[8:9] offset:2560
	global_load_dword v226, v5, s[8:9] offset:3072
	global_load_dword v227, v5, s[8:9] offset:3584
	s_add_u32 s8, s8, 0x1000
	s_addc_u32 s9, s9, 0
	global_load_dword v228, v5, s[8:9]
	global_load_dword v229, v5, s[8:9] offset:512
	global_load_dword v230, v5, s[8:9] offset:1024
	global_load_dword v231, v5, s[8:9] offset:1536
	global_load_dword v232, v5, s[8:9] offset:2048
	global_load_dword v233, v5, s[8:9] offset:2560
	global_load_dword v234, v5, s[8:9] offset:3072
	global_load_dword v235, v5, s[8:9] offset:3584
	s_add_u32 s8, s8, 0x1000
	s_addc_u32 s9, s9, 0
	global_load_dword v236, v5, s[8:9]
	global_load_dword v237, v5, s[8:9] offset:512
	global_load_dword v238, v5, s[8:9] offset:1024
	global_load_dword v239, v5, s[8:9] offset:1536
	global_load_dword v240, v5, s[8:9] offset:2048
	global_load_dword v241, v5, s[8:9] offset:2560
	global_load_dword v242, v5, s[8:9] offset:3072
	global_load_dword v243, v5, s[8:9] offset:3584
	s_add_u32 s8, s8, 0x1000
	s_addc_u32 s9, s9, 0
	global_load_dword v244, v5, s[8:9]
	global_load_dword v245, v5, s[8:9] offset:512
	global_load_dword v246, v5, s[8:9] offset:1024
	global_load_dword v247, v5, s[8:9] offset:1536
	global_load_dword v248, v5, s[8:9] offset:2048
	global_load_dword v249, v5, s[8:9] offset:2560
	global_load_dword v250, v5, s[8:9] offset:3072
	global_load_dword v251, v5, s[8:9] offset:3584
	s_mul_i32 s16, s15, 0x1800
	s_add_u32 s10, s6, s16
	s_addc_u32 s11, s7, 0
	s_lshl_b32 s17, s15, 1
	v_add_u32_e32 v11, s17, v10
	v_mov_b32_e32 v12, 0
	global_load_dwordx4 v[68:71], v9, s[10:11]
	global_load_dwordx4 v[72:75], v9, s[10:11] offset:16
	global_load_dwordx4 v[76:79], v9, s[10:11] offset:32
	global_load_dwordx4 v[80:83], v9, s[10:11] offset:48
	global_load_dwordx4 v[84:87], v9, s[10:11] offset:64
	global_load_dwordx4 v[88:91], v9, s[10:11] offset:80
	global_load_dwordx4 v[92:95], v9, s[10:11] offset:96
	global_load_dwordx4 v[96:99], v9, s[10:11] offset:112
	global_load_dwordx4 v[100:103], v9, s[10:11] offset:128
	global_load_dwordx4 v[104:107], v9, s[10:11] offset:144
	global_load_dwordx4 v[108:111], v9, s[10:11] offset:160
	global_load_dwordx4 v[112:115], v9, s[10:11] offset:176
	s_waitcnt vmcnt(8)
	v_fmac_f32_e32 v12, v68, v124
	v_fmac_f32_e32 v12, v69, v125
	v_fmac_f32_e32 v12, v70, v126
	v_fmac_f32_e32 v12, v71, v127
	v_fmac_f32_e32 v12, v72, v128
	v_fmac_f32_e32 v12, v73, v129
	v_fmac_f32_e32 v12, v74, v130
	v_fmac_f32_e32 v12, v75, v131
	v_fmac_f32_e32 v12, v76, v132
	v_fmac_f32_e32 v12, v77, v133
	v_fmac_f32_e32 v12, v78, v134
	v_fmac_f32_e32 v12, v79, v135
	v_fmac_f32_e32 v12, v80, v136
	v_fmac_f32_e32 v12, v81, v137
	v_fmac_f32_e32 v12, v82, v138
	v_fmac_f32_e32 v12, v83, v139
	global_load_dwordx4 v[68:71], v9, s[10:11] offset:192
	global_load_dwordx4 v[72:75], v9, s[10:11] offset:208
	global_load_dwordx4 v[76:79], v9, s[10:11] offset:224
	global_load_dwordx4 v[80:83], v9, s[10:11] offset:240
	s_waitcnt vmcnt(8)
	v_fmac_f32_e32 v12, v84, v140
	v_fmac_f32_e32 v12, v85, v141
	v_fmac_f32_e32 v12, v86, v142
	v_fmac_f32_e32 v12, v87, v143
	v_fmac_f32_e32 v12, v88, v144
	v_fmac_f32_e32 v12, v89, v145
	v_fmac_f32_e32 v12, v90, v146
	v_fmac_f32_e32 v12, v91, v147
	v_fmac_f32_e32 v12, v92, v148
	v_fmac_f32_e32 v12, v93, v149
	v_fmac_f32_e32 v12, v94, v150
	v_fmac_f32_e32 v12, v95, v151
	v_fmac_f32_e32 v12, v96, v152
	v_fmac_f32_e32 v12, v97, v153
	v_fmac_f32_e32 v12, v98, v154
	v_fmac_f32_e32 v12, v99, v155
	global_load_dwordx4 v[84:87], v9, s[10:11] offset:256
	global_load_dwordx4 v[88:91], v9, s[10:11] offset:272
	global_load_dwordx4 v[92:95], v9, s[10:11] offset:288
	global_load_dwordx4 v[96:99], v9, s[10:11] offset:304
	s_waitcnt vmcnt(8)
	v_fmac_f32_e32 v12, v100, v156
	v_fmac_f32_e32 v12, v101, v157
	v_fmac_f32_e32 v12, v102, v158
	v_fmac_f32_e32 v12, v103, v159
	v_fmac_f32_e32 v12, v104, v160
	v_fmac_f32_e32 v12, v105, v161
	v_fmac_f32_e32 v12, v106, v162
	v_fmac_f32_e32 v12, v107, v163
	v_fmac_f32_e32 v12, v108, v164
	v_fmac_f32_e32 v12, v109, v165
	v_fmac_f32_e32 v12, v110, v166
	v_fmac_f32_e32 v12, v111, v167
	v_fmac_f32_e32 v12, v112, v168
	v_fmac_f32_e32 v12, v113, v169
	v_fmac_f32_e32 v12, v114, v170
	v_fmac_f32_e32 v12, v115, v171
	global_load_dwordx4 v[100:103], v9, s[10:11] offset:320
	global_load_dwordx4 v[104:107], v9, s[10:11] offset:336
	global_load_dwordx4 v[108:111], v9, s[10:11] offset:352
	global_load_dwordx4 v[112:115], v9, s[10:11] offset:368
	s_waitcnt vmcnt(8)
	v_fmac_f32_e32 v12, v68, v172
	v_fmac_f32_e32 v12, v69, v173
	v_fmac_f32_e32 v12, v70, v174
	v_fmac_f32_e32 v12, v71, v175
	v_fmac_f32_e32 v12, v72, v176
	v_fmac_f32_e32 v12, v73, v177
	v_fmac_f32_e32 v12, v74, v178
	v_fmac_f32_e32 v12, v75, v179
	v_fmac_f32_e32 v12, v76, v180
	v_fmac_f32_e32 v12, v77, v181
	v_fmac_f32_e32 v12, v78, v182
	v_fmac_f32_e32 v12, v79, v183
	v_fmac_f32_e32 v12, v80, v184
	v_fmac_f32_e32 v12, v81, v185
	v_fmac_f32_e32 v12, v82, v186
	v_fmac_f32_e32 v12, v83, v187
	global_load_dwordx4 v[68:71], v9, s[10:11] offset:384
	global_load_dwordx4 v[72:75], v9, s[10:11] offset:400
	global_load_dwordx4 v[76:79], v9, s[10:11] offset:416
	global_load_dwordx4 v[80:83], v9, s[10:11] offset:432
	s_waitcnt vmcnt(8)
; __device__ __forceinline__ bf16_t f2bf(float f) { unsigned u = __float_as_uint(f); return (bf16_t)((u + 0x7fffu + ((u >> 16) & 1u)) >> 16); }
; __device__ __forceinline__ void ph_prologue(const Args& a, LAS unsigned char* lds) {
;     ...
;         const float* win = a.in[1]; const float* mix = a.in[2]; const float* psc = a.in[3]; bf16_t* WIN0 = (bf16_t*)(a.ws + WS_WIN0);
;         for (int i = gt; i < 512 * 1024; i += ngt) { const int n = i & 511, k = i >> 9, g = n >> 7, nn = n & 127;
;             const float* wr_ = win + (size_t)k * 1536 + g * 128; const float* mx = mix + (size_t)g * 128 * 128 + nn;
;             float s = 0.f;
;             for (int c = 0; c < 128; ++c) s += wr_[c] * mx[(size_t)c * 128];
;             WIN0[(size_t)n * 1024 + k] = f2bf(s * psc[n]); }
	v_fmac_f32_e32 v12, v84, v188
	v_fmac_f32_e32 v12, v85, v189
	v_fmac_f32_e32 v12, v86, v190
	v_fmac_f32_e32 v12, v87, v191
	v_fmac_f32_e32 v12, v88, v192
	v_fmac_f32_e32 v12, v89, v193
	v_fmac_f32_e32 v12, v90, v194
	v_fmac_f32_e32 v12, v91, v195
	v_fmac_f32_e32 v12, v92, v196
	v_fmac_f32_e32 v12, v93, v197
	v_fmac_f32_e32 v12, v94, v198
	v_fmac_f32_e32 v12, v95, v199
	v_fmac_f32_e32 v12, v96, v200
	v_fmac_f32_e32 v12, v97, v201
	v_fmac_f32_e32 v12, v98, v202
	v_fmac_f32_e32 v12, v99, v203
	global_load_dwordx4 v[84:87], v9, s[10:11] offset:448
	global_load_dwordx4 v[88:91], v9, s[10:11] offset:464
	global_load_dwordx4 v[92:95], v9, s[10:11] offset:480
	global_load_dwordx4 v[96:99], v9, s[10:11] offset:496
	s_waitcnt vmcnt(8)
	v_fmac_f32_e32 v12, v100, v204
	v_fmac_f32_e32 v12, v101, v205
	v_fmac_f32_e32 v12, v102, v206
	v_fmac_f32_e32 v12, v103, v207
	v_fmac_f32_e32 v12, v104, v208
	v_fmac_f32_e32 v12, v105, v209
	v_fmac_f32_e32 v12, v106, v210
	v_fmac_f32_e32 v12, v107, v211
	v_fmac_f32_e32 v12, v108, v212
	v_fmac_f32_e32 v12, v109, v213
	v_fmac_f32_e32 v12, v110, v214
	v_fmac_f32_e32 v12, v111, v215
	v_fmac_f32_e32 v12, v112, v216
	v_fmac_f32_e32 v12, v113, v217
	v_fmac_f32_e32 v12, v114, v218
	v_fmac_f32_e32 v12, v115, v219
	s_add_u32 s10, s10, 0x180000
	s_addc_u32 s11, s11, 0
	global_load_dwordx4 v[100:103], v9, s[10:11]
	global_load_dwordx4 v[104:107], v9, s[10:11] offset:16
	global_load_dwordx4 v[108:111], v9, s[10:11] offset:32
	global_load_dwordx4 v[112:115], v9, s[10:11] offset:48
	s_waitcnt vmcnt(8)
	v_fmac_f32_e32 v12, v68, v220
	v_fmac_f32_e32 v12, v69, v221
	v_fmac_f32_e32 v12, v70, v222
	v_fmac_f32_e32 v12, v71, v223
	v_fmac_f32_e32 v12, v72, v224
	v_fmac_f32_e32 v12, v73, v225
	v_fmac_f32_e32 v12, v74, v226
	v_fmac_f32_e32 v12, v75, v227
	v_fmac_f32_e32 v12, v76, v228
	v_fmac_f32_e32 v12, v77, v229
	v_fmac_f32_e32 v12, v78, v230
	v_fmac_f32_e32 v12, v79, v231
	v_fmac_f32_e32 v12, v80, v232
	v_fmac_f32_e32 v12, v81, v233
	v_fmac_f32_e32 v12, v82, v234
	v_fmac_f32_e32 v12, v83, v235
	global_load_dwordx4 v[68:71], v9, s[10:11] offset:64
	global_load_dwordx4 v[72:75], v9, s[10:11] offset:80
	global_load_dwordx4 v[76:79], v9, s[10:11] offset:96
	global_load_dwordx4 v[80:83], v9, s[10:11] offset:112
	s_waitcnt vmcnt(8)
	v_fmac_f32_e32 v12, v84, v236
	v_fmac_f32_e32 v12, v85, v237
	v_fmac_f32_e32 v12, v86, v238
	v_fmac_f32_e32 v12, v87, v239
	v_fmac_f32_e32 v12, v88, v240
	v_fmac_f32_e32 v12, v89, v241
	v_fmac_f32_e32 v12, v90, v242
	v_fmac_f32_e32 v12, v91, v243
	v_fmac_f32_e32 v12, v92, v244
	v_fmac_f32_e32 v12, v93, v245
	v_fmac_f32_e32 v12, v94, v246
	v_fmac_f32_e32 v12, v95, v247
	v_fmac_f32_e32 v12, v96, v248
	v_fmac_f32_e32 v12, v97, v249
	v_fmac_f32_e32 v12, v98, v250
	v_fmac_f32_e32 v12, v99, v251
	v_mul_f32_e32 v13, v7, v12
	v_bfe_u32 v14, v13, 16, 1
	v_add3_u32 v13, v13, v14, s14
	global_store_short_d16_hi v11, v13, s[12:13]
	v_add_u32_e32 v11, 0x200, v11
	v_mov_b32_e32 v12, 0
	global_load_dwordx4 v[84:87], v9, s[10:11] offset:128
	global_load_dwordx4 v[88:91], v9, s[10:11] offset:144
	global_load_dwordx4 v[92:95], v9, s[10:11] offset:160
	global_load_dwordx4 v[96:99], v9, s[10:11] offset:176
	s_waitcnt vmcnt(9)
	v_fmac_f32_e32 v12, v100, v124
	v_fmac_f32_e32 v12, v101, v125
	v_fmac_f32_e32 v12, v102, v126
	v_fmac_f32_e32 v12, v103, v127
	v_fmac_f32_e32 v12, v104, v128
	v_fmac_f32_e32 v12, v105, v129
	v_fmac_f32_e32 v12, v106, v130
	v_fmac_f32_e32 v12, v107, v131
	v_fmac_f32_e32 v12, v108, v132
	v_fmac_f32_e32 v12, v109, v133
	v_fmac_f32_e32 v12, v110, v134
	v_fmac_f32_e32 v12, v111, v135
	v_fmac_f32_e32 v12, v112, v136
	v_fmac_f32_e32 v12, v113, v137
	v_fmac_f32_e32 v12, v114, v138
	v_fmac_f32_e32 v12, v115, v139
	global_load_dwordx4 v[100:103], v9, s[10:11] offset:192
	global_load_dwordx4 v[104:107], v9, s[10:11] offset:208
	global_load_dwordx4 v[108:111], v9, s[10:11] offset:224
	global_load_dwordx4 v[112:115], v9, s[10:11] offset:240
	s_waitcnt vmcnt(9)
	v_fmac_f32_e32 v12, v68, v140
	v_fmac_f32_e32 v12, v69, v141
	v_fmac_f32_e32 v12, v70, v142
	v_fmac_f32_e32 v12, v71, v143
	v_fmac_f32_e32 v12, v72, v144
	v_fmac_f32_e32 v12, v73, v145
	v_fmac_f32_e32 v12, v74, v146
	v_fmac_f32_e32 v12, v75, v147
	v_fmac_f32_e32 v12, v76, v148
	v_fmac_f32_e32 v12, v77, v149
	v_fmac_f32_e32 v12, v78, v150
	v_fmac_f32_e32 v12, v79, v151
	v_fmac_f32_e32 v12, v80, v152
	v_fmac_f32_e32 v12, v81, v153
	v_fmac_f32_e32 v12, v82, v154
	v_fmac_f32_e32 v12, v83, v155
	global_load_dwordx4 v[68:71], v9, s[10:11] offset:256
	global_load_dwordx4 v[72:75], v9, s[10:11] offset:272
	global_load_dwordx4 v[76:79], v9, s[10:11] offset:288
	global_load_dwordx4 v[80:83], v9, s[10:11] offset:304
	s_waitcnt vmcnt(8)
	v_fmac_f32_e32 v12, v84, v156
	v_fmac_f32_e32 v12, v85, v157
	v_fmac_f32_e32 v12, v86, v158
	v_fmac_f32_e32 v12, v87, v159
	v_fmac_f32_e32 v12, v88, v160
	v_fmac_f32_e32 v12, v89, v161
	v_fmac_f32_e32 v12, v90, v162
	v_fmac_f32_e32 v12, v91, v163
	v_fmac_f32_e32 v12, v92, v164
	v_fmac_f32_e32 v12, v93, v165
	v_fmac_f32_e32 v12, v94, v166
	v_fmac_f32_e32 v12, v95, v167
	v_fmac_f32_e32 v12, v96, v168
	v_fmac_f32_e32 v12, v97, v169
	v_fmac_f32_e32 v12, v98, v170
	v_fmac_f32_e32 v12, v99, v171
	global_load_dwordx4 v[84:87], v9, s[10:11] offset:320
	global_load_dwordx4 v[88:91], v9, s[10:11] offset:336
	global_load_dwordx4 v[92:95], v9, s[10:11] offset:352
	global_load_dwordx4 v[96:99], v9, s[10:11] offset:368
	s_waitcnt vmcnt(8)
; __device__ __forceinline__ bf16_t f2bf(float f) { unsigned u = __float_as_uint(f); return (bf16_t)((u + 0x7fffu + ((u >> 16) & 1u)) >> 16); }
; __device__ __forceinline__ void ph_prologue(const Args& a, LAS unsigned char* lds) {
;     ...
;         const float* win = a.in[1]; const float* mix = a.in[2]; const float* psc = a.in[3]; bf16_t* WIN0 = (bf16_t*)(a.ws + WS_WIN0);
;         for (int i = gt; i < 512 * 1024; i += ngt) { const int n = i & 511, k = i >> 9, g = n >> 7, nn = n & 127;
;             const float* wr_ = win + (size_t)k * 1536 + g * 128; const float* mx = mix + (size_t)g * 128 * 128 + nn;
;             float s = 0.f;
;             for (int c = 0; c < 128; ++c) s += wr_[c] * mx[(size_t)c * 128];
;             WIN0[(size_t)n * 1024 + k] = f2bf(s * psc[n]); }
	v_fmac_f32_e32 v12, v100, v172
	v_fmac_f32_e32 v12, v101, v173
	v_fmac_f32_e32 v12, v102, v174
	v_fmac_f32_e32 v12, v103, v175
	v_fmac_f32_e32 v12, v104, v176
	v_fmac_f32_e32 v12, v105, v177
	v_fmac_f32_e32 v12, v106, v178
	v_fmac_f32_e32 v12, v107, v179
	v_fmac_f32_e32 v12, v108, v180
	v_fmac_f32_e32 v12, v109, v181
	v_fmac_f32_e32 v12, v110, v182
	v_fmac_f32_e32 v12, v111, v183
	v_fmac_f32_e32 v12, v112, v184
	v_fmac_f32_e32 v12, v113, v185
	v_fmac_f32_e32 v12, v114, v186
	v_fmac_f32_e32 v12, v115, v187
	global_load_dwordx4 v[100:103], v9, s[10:11] offset:384
	global_load_dwordx4 v[104:107], v9, s[10:11] offset:400
	global_load_dwordx4 v[108:111], v9, s[10:11] offset:416
	global_load_dwordx4 v[112:115], v9, s[10:11] offset:432
	s_waitcnt vmcnt(8)
	v_fmac_f32_e32 v12, v68, v188
	v_fmac_f32_e32 v12, v69, v189
	v_fmac_f32_e32 v12, v70, v190
	v_fmac_f32_e32 v12, v71, v191
	v_fmac_f32_e32 v12, v72, v192
	v_fmac_f32_e32 v12, v73, v193
	v_fmac_f32_e32 v12, v74, v194
	v_fmac_f32_e32 v12, v75, v195
	v_fmac_f32_e32 v12, v76, v196
	v_fmac_f32_e32 v12, v77, v197
	v_fmac_f32_e32 v12, v78, v198
	v_fmac_f32_e32 v12, v79, v199
	v_fmac_f32_e32 v12, v80, v200
	v_fmac_f32_e32 v12, v81, v201
	v_fmac_f32_e32 v12, v82, v202
	v_fmac_f32_e32 v12, v83, v203
	global_load_dwordx4 v[68:71], v9, s[10:11] offset:448
	global_load_dwordx4 v[72:75], v9, s[10:11] offset:464
	global_load_dwordx4 v[76:79], v9, s[10:11] offset:480
	global_load_dwordx4 v[80:83], v9, s[10:11] offset:496
	s_waitcnt vmcnt(8)
	v_fmac_f32_e32 v12, v84, v204
	v_fmac_f32_e32 v12, v85, v205
	v_fmac_f32_e32 v12, v86, v206
	v_fmac_f32_e32 v12, v87, v207
	v_fmac_f32_e32 v12, v88, v208
	v_fmac_f32_e32 v12, v89, v209
	v_fmac_f32_e32 v12, v90, v210
	v_fmac_f32_e32 v12, v91, v211
	v_fmac_f32_e32 v12, v92, v212
	v_fmac_f32_e32 v12, v93, v213
	v_fmac_f32_e32 v12, v94, v214
	v_fmac_f32_e32 v12, v95, v215
	v_fmac_f32_e32 v12, v96, v216
	v_fmac_f32_e32 v12, v97, v217
	v_fmac_f32_e32 v12, v98, v218
	v_fmac_f32_e32 v12, v99, v219
	s_add_u32 s10, s10, 0x180000
	s_addc_u32 s11, s11, 0
	global_load_dwordx4 v[84:87], v9, s[10:11]
	global_load_dwordx4 v[88:91], v9, s[10:11] offset:16
	global_load_dwordx4 v[92:95], v9, s[10:11] offset:32
	global_load_dwordx4 v[96:99], v9, s[10:11] offset:48
	s_waitcnt vmcnt(8)
	v_fmac_f32_e32 v12, v100, v220
	v_fmac_f32_e32 v12, v101, v221
	v_fmac_f32_e32 v12, v102, v222
	v_fmac_f32_e32 v12, v103, v223
	v_fmac_f32_e32 v12, v104, v224
	v_fmac_f32_e32 v12, v105, v225
	v_fmac_f32_e32 v12, v106, v226
	v_fmac_f32_e32 v12, v107, v227
	v_fmac_f32_e32 v12, v108, v228
	v_fmac_f32_e32 v12, v109, v229
	v_fmac_f32_e32 v12, v110, v230
	v_fmac_f32_e32 v12, v111, v231
	v_fmac_f32_e32 v12, v112, v232
	v_fmac_f32_e32 v12, v113, v233
	v_fmac_f32_e32 v12, v114, v234
	v_fmac_f32_e32 v12, v115, v235
	global_load_dwordx4 v[100:103], v9, s[10:11] offset:64
	global_load_dwordx4 v[104:107], v9, s[10:11] offset:80
	global_load_dwordx4 v[108:111], v9, s[10:11] offset:96
	global_load_dwordx4 v[112:115], v9, s[10:11] offset:112
	s_waitcnt vmcnt(8)
	v_fmac_f32_e32 v12, v68, v236
	v_fmac_f32_e32 v12, v69, v237
	v_fmac_f32_e32 v12, v70, v238
	v_fmac_f32_e32 v12, v71, v239
	v_fmac_f32_e32 v12, v72, v240
	v_fmac_f32_e32 v12, v73, v241
	v_fmac_f32_e32 v12, v74, v242
	v_fmac_f32_e32 v12, v75, v243
	v_fmac_f32_e32 v12, v76, v244
	v_fmac_f32_e32 v12, v77, v245
	v_fmac_f32_e32 v12, v78, v246
	v_fmac_f32_e32 v12, v79, v247
	v_fmac_f32_e32 v12, v80, v248
	v_fmac_f32_e32 v12, v81, v249
	v_fmac_f32_e32 v12, v82, v250
	v_fmac_f32_e32 v12, v83, v251
	v_mul_f32_e32 v13, v7, v12
	v_bfe_u32 v14, v13, 16, 1
	v_add3_u32 v13, v13, v14, s14
	global_store_short_d16_hi v11, v13, s[12:13]
	v_add_u32_e32 v11, 0x200, v11
	v_mov_b32_e32 v12, 0
	global_load_dwordx4 v[68:71], v9, s[10:11] offset:128
	global_load_dwordx4 v[72:75], v9, s[10:11] offset:144
	global_load_dwordx4 v[76:79], v9, s[10:11] offset:160
	global_load_dwordx4 v[80:83], v9, s[10:11] offset:176
	s_waitcnt vmcnt(9)
	v_fmac_f32_e32 v12, v84, v124
	v_fmac_f32_e32 v12, v85, v125
	v_fmac_f32_e32 v12, v86, v126
	v_fmac_f32_e32 v12, v87, v127
	v_fmac_f32_e32 v12, v88, v128
	v_fmac_f32_e32 v12, v89, v129
	v_fmac_f32_e32 v12, v90, v130
	v_fmac_f32_e32 v12, v91, v131
	v_fmac_f32_e32 v12, v92, v132
	v_fmac_f32_e32 v12, v93, v133
	v_fmac_f32_e32 v12, v94, v134
	v_fmac_f32_e32 v12, v95, v135
	v_fmac_f32_e32 v12, v96, v136
	v_fmac_f32_e32 v12, v97, v137
	v_fmac_f32_e32 v12, v98, v138
	v_fmac_f32_e32 v12, v99, v139
	global_load_dwordx4 v[84:87], v9, s[10:11] offset:192
	global_load_dwordx4 v[88:91], v9, s[10:11] offset:208
	global_load_dwordx4 v[92:95], v9, s[10:11] offset:224
	global_load_dwordx4 v[96:99], v9, s[10:11] offset:240
	s_waitcnt vmcnt(9)
	v_fmac_f32_e32 v12, v100, v140
	v_fmac_f32_e32 v12, v101, v141
	v_fmac_f32_e32 v12, v102, v142
	v_fmac_f32_e32 v12, v103, v143
	v_fmac_f32_e32 v12, v104, v144
	v_fmac_f32_e32 v12, v105, v145
	v_fmac_f32_e32 v12, v106, v146
	v_fmac_f32_e32 v12, v107, v147
	v_fmac_f32_e32 v12, v108, v148
	v_fmac_f32_e32 v12, v109, v149
	v_fmac_f32_e32 v12, v110, v150
	v_fmac_f32_e32 v12, v111, v151
	v_fmac_f32_e32 v12, v112, v152
	v_fmac_f32_e32 v12, v113, v153
	v_fmac_f32_e32 v12, v114, v154
	v_fmac_f32_e32 v12, v115, v155
	global_load_dwordx4 v[100:103], v9, s[10:11] offset:256
	global_load_dwordx4 v[104:107], v9, s[10:11] offset:272
	global_load_dwordx4 v[108:111], v9, s[10:11] offset:288
	global_load_dwordx4 v[112:115], v9, s[10:11] offset:304
	s_waitcnt vmcnt(8)
; __device__ __forceinline__ bf16_t f2bf(float f) { unsigned u = __float_as_uint(f); return (bf16_t)((u + 0x7fffu + ((u >> 16) & 1u)) >> 16); }
; __device__ __forceinline__ void ph_prologue(const Args& a, LAS unsigned char* lds) {
;     ...
;         const float* win = a.in[1]; const float* mix = a.in[2]; const float* psc = a.in[3]; bf16_t* WIN0 = (bf16_t*)(a.ws + WS_WIN0);
;         for (int i = gt; i < 512 * 1024; i += ngt) { const int n = i & 511, k = i >> 9, g = n >> 7, nn = n & 127;
;             const float* wr_ = win + (size_t)k * 1536 + g * 128; const float* mx = mix + (size_t)g * 128 * 128 + nn;
;             float s = 0.f;
;             for (int c = 0; c < 128; ++c) s += wr_[c] * mx[(size_t)c * 128];
;             WIN0[(size_t)n * 1024 + k] = f2bf(s * psc[n]); }
	v_fmac_f32_e32 v12, v68, v156
	v_fmac_f32_e32 v12, v69, v157
	v_fmac_f32_e32 v12, v70, v158
	v_fmac_f32_e32 v12, v71, v159
	v_fmac_f32_e32 v12, v72, v160
	v_fmac_f32_e32 v12, v73, v161
	v_fmac_f32_e32 v12, v74, v162
	v_fmac_f32_e32 v12, v75, v163
	v_fmac_f32_e32 v12, v76, v164
	v_fmac_f32_e32 v12, v77, v165
	v_fmac_f32_e32 v12, v78, v166
	v_fmac_f32_e32 v12, v79, v167
	v_fmac_f32_e32 v12, v80, v168
	v_fmac_f32_e32 v12, v81, v169
	v_fmac_f32_e32 v12, v82, v170
	v_fmac_f32_e32 v12, v83, v171
	global_load_dwordx4 v[68:71], v9, s[10:11] offset:320
	global_load_dwordx4 v[72:75], v9, s[10:11] offset:336
	global_load_dwordx4 v[76:79], v9, s[10:11] offset:352
	global_load_dwordx4 v[80:83], v9, s[10:11] offset:368
	s_waitcnt vmcnt(8)
	v_fmac_f32_e32 v12, v84, v172
	v_fmac_f32_e32 v12, v85, v173
	v_fmac_f32_e32 v12, v86, v174
	v_fmac_f32_e32 v12, v87, v175
	v_fmac_f32_e32 v12, v88, v176
	v_fmac_f32_e32 v12, v89, v177
	v_fmac_f32_e32 v12, v90, v178
	v_fmac_f32_e32 v12, v91, v179
	v_fmac_f32_e32 v12, v92, v180
	v_fmac_f32_e32 v12, v93, v181
	v_fmac_f32_e32 v12, v94, v182
	v_fmac_f32_e32 v12, v95, v183
	v_fmac_f32_e32 v12, v96, v184
	v_fmac_f32_e32 v12, v97, v185
	v_fmac_f32_e32 v12, v98, v186
	v_fmac_f32_e32 v12, v99, v187
	global_load_dwordx4 v[84:87], v9, s[10:11] offset:384
	global_load_dwordx4 v[88:91], v9, s[10:11] offset:400
	global_load_dwordx4 v[92:95], v9, s[10:11] offset:416
	global_load_dwordx4 v[96:99], v9, s[10:11] offset:432
	s_waitcnt vmcnt(8)
	v_fmac_f32_e32 v12, v100, v188
	v_fmac_f32_e32 v12, v101, v189
	v_fmac_f32_e32 v12, v102, v190
	v_fmac_f32_e32 v12, v103, v191
	v_fmac_f32_e32 v12, v104, v192
	v_fmac_f32_e32 v12, v105, v193
	v_fmac_f32_e32 v12, v106, v194
	v_fmac_f32_e32 v12, v107, v195
	v_fmac_f32_e32 v12, v108, v196
	v_fmac_f32_e32 v12, v109, v197
	v_fmac_f32_e32 v12, v110, v198
	v_fmac_f32_e32 v12, v111, v199
	v_fmac_f32_e32 v12, v112, v200
	v_fmac_f32_e32 v12, v113, v201
	v_fmac_f32_e32 v12, v114, v202
	v_fmac_f32_e32 v12, v115, v203
	global_load_dwordx4 v[100:103], v9, s[10:11] offset:448
	global_load_dwordx4 v[104:107], v9, s[10:11] offset:464
	global_load_dwordx4 v[108:111], v9, s[10:11] offset:480
	global_load_dwordx4 v[112:115], v9, s[10:11] offset:496
	s_waitcnt vmcnt(8)
	v_fmac_f32_e32 v12, v68, v204
	v_fmac_f32_e32 v12, v69, v205
	v_fmac_f32_e32 v12, v70, v206
	v_fmac_f32_e32 v12, v71, v207
	v_fmac_f32_e32 v12, v72, v208
	v_fmac_f32_e32 v12, v73, v209
	v_fmac_f32_e32 v12, v74, v210
	v_fmac_f32_e32 v12, v75, v211
	v_fmac_f32_e32 v12, v76, v212
	v_fmac_f32_e32 v12, v77, v213
	v_fmac_f32_e32 v12, v78, v214
	v_fmac_f32_e32 v12, v79, v215
	v_fmac_f32_e32 v12, v80, v216
	v_fmac_f32_e32 v12, v81, v217
	v_fmac_f32_e32 v12, v82, v218
	v_fmac_f32_e32 v12, v83, v219
	s_add_u32 s10, s10, 0x180000
	s_addc_u32 s11, s11, 0
	global_load_dwordx4 v[68:71], v9, s[10:11]
	global_load_dwordx4 v[72:75], v9, s[10:11] offset:16
	global_load_dwordx4 v[76:79], v9, s[10:11] offset:32
	global_load_dwordx4 v[80:83], v9, s[10:11] offset:48
	s_waitcnt vmcnt(8)
	v_fmac_f32_e32 v12, v84, v220
	v_fmac_f32_e32 v12, v85, v221
	v_fmac_f32_e32 v12, v86, v222
	v_fmac_f32_e32 v12, v87, v223
	v_fmac_f32_e32 v12, v88, v224
	v_fmac_f32_e32 v12, v89, v225
	v_fmac_f32_e32 v12, v90, v226
	v_fmac_f32_e32 v12, v91, v227
	v_fmac_f32_e32 v12, v92, v228
	v_fmac_f32_e32 v12, v93, v229
	v_fmac_f32_e32 v12, v94, v230
	v_fmac_f32_e32 v12, v95, v231
	v_fmac_f32_e32 v12, v96, v232
	v_fmac_f32_e32 v12, v97, v233
	v_fmac_f32_e32 v12, v98, v234
	v_fmac_f32_e32 v12, v99, v235
	global_load_dwordx4 v[84:87], v9, s[10:11] offset:64
	global_load_dwordx4 v[88:91], v9, s[10:11] offset:80
	global_load_dwordx4 v[92:95], v9, s[10:11] offset:96
	global_load_dwordx4 v[96:99], v9, s[10:11] offset:112
	s_waitcnt vmcnt(8)
	v_fmac_f32_e32 v12, v100, v236
	v_fmac_f32_e32 v12, v101, v237
	v_fmac_f32_e32 v12, v102, v238
	v_fmac_f32_e32 v12, v103, v239
	v_fmac_f32_e32 v12, v104, v240
	v_fmac_f32_e32 v12, v105, v241
	v_fmac_f32_e32 v12, v106, v242
	v_fmac_f32_e32 v12, v107, v243
	v_fmac_f32_e32 v12, v108, v244
	v_fmac_f32_e32 v12, v109, v245
	v_fmac_f32_e32 v12, v110, v246
	v_fmac_f32_e32 v12, v111, v247
	v_fmac_f32_e32 v12, v112, v248
	v_fmac_f32_e32 v12, v113, v249
	v_fmac_f32_e32 v12, v114, v250
	v_fmac_f32_e32 v12, v115, v251
	v_mul_f32_e32 v13, v7, v12
	v_bfe_u32 v14, v13, 16, 1
	v_add3_u32 v13, v13, v14, s14
	global_store_short_d16_hi v11, v13, s[12:13]
	v_add_u32_e32 v11, 0x200, v11
	v_mov_b32_e32 v12, 0
	global_load_dwordx4 v[100:103], v9, s[10:11] offset:128
	global_load_dwordx4 v[104:107], v9, s[10:11] offset:144
	global_load_dwordx4 v[108:111], v9, s[10:11] offset:160
	global_load_dwordx4 v[112:115], v9, s[10:11] offset:176
	s_waitcnt vmcnt(9)
	v_fmac_f32_e32 v12, v68, v124
	v_fmac_f32_e32 v12, v69, v125
	v_fmac_f32_e32 v12, v70, v126
	v_fmac_f32_e32 v12, v71, v127
	v_fmac_f32_e32 v12, v72, v128
	v_fmac_f32_e32 v12, v73, v129
	v_fmac_f32_e32 v12, v74, v130
	v_fmac_f32_e32 v12, v75, v131
	v_fmac_f32_e32 v12, v76, v132
	v_fmac_f32_e32 v12, v77, v133
	v_fmac_f32_e32 v12, v78, v134
	v_fmac_f32_e32 v12, v79, v135
	v_fmac_f32_e32 v12, v80, v136
	v_fmac_f32_e32 v12, v81, v137
	v_fmac_f32_e32 v12, v82, v138
	v_fmac_f32_e32 v12, v83, v139
	global_load_dwordx4 v[68:71], v9, s[10:11] offset:192
	global_load_dwordx4 v[72:75], v9, s[10:11] offset:208
	global_load_dwordx4 v[76:79], v9, s[10:11] offset:224
	global_load_dwordx4 v[80:83], v9, s[10:11] offset:240
	s_waitcnt vmcnt(9)
; __device__ __forceinline__ bf16_t f2bf(float f) { unsigned u = __float_as_uint(f); return (bf16_t)((u + 0x7fffu + ((u >> 16) & 1u)) >> 16); }
; __device__ __forceinline__ void ph_prologue(const Args& a, LAS unsigned char* lds) {
;     ...
;         const float* win = a.in[1]; const float* mix = a.in[2]; const float* psc = a.in[3]; bf16_t* WIN0 = (bf16_t*)(a.ws + WS_WIN0);
;         for (int i = gt; i < 512 * 1024; i += ngt) { const int n = i & 511, k = i >> 9, g = n >> 7, nn = n & 127;
;             const float* wr_ = win + (size_t)k * 1536 + g * 128; const float* mx = mix + (size_t)g * 128 * 128 + nn;
;             float s = 0.f;
;             for (int c = 0; c < 128; ++c) s += wr_[c] * mx[(size_t)c * 128];
;             WIN0[(size_t)n * 1024 + k] = f2bf(s * psc[n]); }
	v_fmac_f32_e32 v12, v84, v140
	v_fmac_f32_e32 v12, v85, v141
	v_fmac_f32_e32 v12, v86, v142
	v_fmac_f32_e32 v12, v87, v143
	v_fmac_f32_e32 v12, v88, v144
	v_fmac_f32_e32 v12, v89, v145
	v_fmac_f32_e32 v12, v90, v146
	v_fmac_f32_e32 v12, v91, v147
	v_fmac_f32_e32 v12, v92, v148
	v_fmac_f32_e32 v12, v93, v149
	v_fmac_f32_e32 v12, v94, v150
	v_fmac_f32_e32 v12, v95, v151
	v_fmac_f32_e32 v12, v96, v152
	v_fmac_f32_e32 v12, v97, v153
	v_fmac_f32_e32 v12, v98, v154
	v_fmac_f32_e32 v12, v99, v155
	global_load_dwordx4 v[84:87], v9, s[10:11] offset:256
	global_load_dwordx4 v[88:91], v9, s[10:11] offset:272
	global_load_dwordx4 v[92:95], v9, s[10:11] offset:288
	global_load_dwordx4 v[96:99], v9, s[10:11] offset:304
	s_waitcnt vmcnt(8)
	v_fmac_f32_e32 v12, v100, v156
	v_fmac_f32_e32 v12, v101, v157
	v_fmac_f32_e32 v12, v102, v158
	v_fmac_f32_e32 v12, v103, v159
	v_fmac_f32_e32 v12, v104, v160
	v_fmac_f32_e32 v12, v105, v161
	v_fmac_f32_e32 v12, v106, v162
	v_fmac_f32_e32 v12, v107, v163
	v_fmac_f32_e32 v12, v108, v164
	v_fmac_f32_e32 v12, v109, v165
	v_fmac_f32_e32 v12, v110, v166
	v_fmac_f32_e32 v12, v111, v167
	v_fmac_f32_e32 v12, v112, v168
	v_fmac_f32_e32 v12, v113, v169
	v_fmac_f32_e32 v12, v114, v170
	v_fmac_f32_e32 v12, v115, v171
	global_load_dwordx4 v[100:103], v9, s[10:11] offset:320
	global_load_dwordx4 v[104:107], v9, s[10:11] offset:336
	global_load_dwordx4 v[108:111], v9, s[10:11] offset:352
	global_load_dwordx4 v[112:115], v9, s[10:11] offset:368
	s_waitcnt vmcnt(8)
	v_fmac_f32_e32 v12, v68, v172
	v_fmac_f32_e32 v12, v69, v173
	v_fmac_f32_e32 v12, v70, v174
	v_fmac_f32_e32 v12, v71, v175
	v_fmac_f32_e32 v12, v72, v176
	v_fmac_f32_e32 v12, v73, v177
	v_fmac_f32_e32 v12, v74, v178
	v_fmac_f32_e32 v12, v75, v179
	v_fmac_f32_e32 v12, v76, v180
	v_fmac_f32_e32 v12, v77, v181
	v_fmac_f32_e32 v12, v78, v182
	v_fmac_f32_e32 v12, v79, v183
	v_fmac_f32_e32 v12, v80, v184
	v_fmac_f32_e32 v12, v81, v185
	v_fmac_f32_e32 v12, v82, v186
	v_fmac_f32_e32 v12, v83, v187
	global_load_dwordx4 v[68:71], v9, s[10:11] offset:384
	global_load_dwordx4 v[72:75], v9, s[10:11] offset:400
	global_load_dwordx4 v[76:79], v9, s[10:11] offset:416
	global_load_dwordx4 v[80:83], v9, s[10:11] offset:432
	s_waitcnt vmcnt(8)
	v_fmac_f32_e32 v12, v84, v188
	v_fmac_f32_e32 v12, v85, v189
	v_fmac_f32_e32 v12, v86, v190
	v_fmac_f32_e32 v12, v87, v191
	v_fmac_f32_e32 v12, v88, v192
	v_fmac_f32_e32 v12, v89, v193
	v_fmac_f32_e32 v12, v90, v194
	v_fmac_f32_e32 v12, v91, v195
	v_fmac_f32_e32 v12, v92, v196
	v_fmac_f32_e32 v12, v93, v197
	v_fmac_f32_e32 v12, v94, v198
	v_fmac_f32_e32 v12, v95, v199
	v_fmac_f32_e32 v12, v96, v200
	v_fmac_f32_e32 v12, v97, v201
	v_fmac_f32_e32 v12, v98, v202
	v_fmac_f32_e32 v12, v99, v203
	global_load_dwordx4 v[84:87], v9, s[10:11] offset:448
	global_load_dwordx4 v[88:91], v9, s[10:11] offset:464
	global_load_dwordx4 v[92:95], v9, s[10:11] offset:480
	global_load_dwordx4 v[96:99], v9, s[10:11] offset:496
	s_waitcnt vmcnt(8)
	v_fmac_f32_e32 v12, v100, v204
	v_fmac_f32_e32 v12, v101, v205
	v_fmac_f32_e32 v12, v102, v206
	v_fmac_f32_e32 v12, v103, v207
	v_fmac_f32_e32 v12, v104, v208
	v_fmac_f32_e32 v12, v105, v209
	v_fmac_f32_e32 v12, v106, v210
	v_fmac_f32_e32 v12, v107, v211
	v_fmac_f32_e32 v12, v108, v212
	v_fmac_f32_e32 v12, v109, v213
	v_fmac_f32_e32 v12, v110, v214
	v_fmac_f32_e32 v12, v111, v215
	v_fmac_f32_e32 v12, v112, v216
	v_fmac_f32_e32 v12, v113, v217
	v_fmac_f32_e32 v12, v114, v218
	v_fmac_f32_e32 v12, v115, v219
	s_waitcnt vmcnt(4)
	v_fmac_f32_e32 v12, v68, v220
	v_fmac_f32_e32 v12, v69, v221
	v_fmac_f32_e32 v12, v70, v222
	v_fmac_f32_e32 v12, v71, v223
	v_fmac_f32_e32 v12, v72, v224
	v_fmac_f32_e32 v12, v73, v225
	v_fmac_f32_e32 v12, v74, v226
	v_fmac_f32_e32 v12, v75, v227
	v_fmac_f32_e32 v12, v76, v228
	v_fmac_f32_e32 v12, v77, v229
	v_fmac_f32_e32 v12, v78, v230
	v_fmac_f32_e32 v12, v79, v231
	v_fmac_f32_e32 v12, v80, v232
	v_fmac_f32_e32 v12, v81, v233
	v_fmac_f32_e32 v12, v82, v234
	v_fmac_f32_e32 v12, v83, v235
	s_waitcnt vmcnt(0)
	v_fmac_f32_e32 v12, v84, v236
	v_fmac_f32_e32 v12, v85, v237
	v_fmac_f32_e32 v12, v86, v238
	v_fmac_f32_e32 v12, v87, v239
	v_fmac_f32_e32 v12, v88, v240
	v_fmac_f32_e32 v12, v89, v241
	v_fmac_f32_e32 v12, v90, v242
	v_fmac_f32_e32 v12, v91, v243
	v_fmac_f32_e32 v12, v92, v244
	v_fmac_f32_e32 v12, v93, v245
	v_fmac_f32_e32 v12, v94, v246
	v_fmac_f32_e32 v12, v95, v247
	v_fmac_f32_e32 v12, v96, v248
	v_fmac_f32_e32 v12, v97, v249
	v_fmac_f32_e32 v12, v98, v250
	v_fmac_f32_e32 v12, v99, v251
	v_mul_f32_e32 v13, v7, v12
	v_bfe_u32 v14, v13, 16, 1
	v_add3_u32 v13, v13, v14, s14
	global_store_short_d16_hi v11, v13, s[12:13]
	s_branch .LBB0_95
.Lfold_orig:
	s_mov_b32 s4, 0x80000
	v_cmp_gt_i32_e32 vcc, s4, v8
	s_and_saveexec_b64 s[4:5], vcc
	s_cbranch_execz .LBB0_95
	s_load_dwordx4 s[8:11], s[82:83], 0x10
	s_load_dwordx2 s[6:7], s[82:83], 0x8
	v_lshlrev_b32_e32 v2, 2, v0
	v_and_b32_e32 v9, 0x7f, v0
	v_mov_b32_e32 v3, 0
	s_waitcnt lgkmcnt(0)
	global_load_dword v7, v2, s[10:11]
	v_lshlrev_b32_e32 v2, 11, v0
	v_lshl_add_u64 v[4:5], s[0:1], 0, v[2:3]
	v_lshlrev_b32_e32 v2, 2, v9
	s_mov_b64 s[10:11], 0x3db00000
	v_lshl_add_u64 v[10:11], s[8:9], 0, v[2:3]
	s_mov_b64 s[8:9], 0x1e00
	v_lshlrev_b32_e32 v2, 7, v0
	v_lshl_add_u64 v[4:5], v[4:5], 0, s[10:11]
	v_lshl_add_u64 v[10:11], v[10:11], 0, s[8:9]
	v_lshl_or_b32 v9, s18, 16, v2
	s_lshl_b32 s14, s22, 16
	s_mov_b64 s[8:9], 0
	s_movk_i32 s15, 0x600
	s_movk_i32 s16, 0xf000
	s_mov_b64 s[10:11], 0x2000
	s_movk_i32 s17, 0x7fff
	s_mov_b32 s18, 0x7ffff
	v_mov_b32_e32 v19, v8
